# v37 + per-unit accumulator zeroing with v_pk_mov_b32 pairs (64 instead of 127 moves) in the five GEMM phases
# speedup vs baseline: 1.0012x; 1.0007x over previous
;     ...
; #pragma unroll
;         for (int a = 0; a < 2; ++a)
; #pragma unroll
;             for (int b = 0; b < 2; ++b)
; #pragma unroll
;                 for (int m = 0; m < 4; ++m)
; #pragma unroll
;                     for (int n = 0; n < 2; ++n) acc[a][b][m][n] = (f32x4){0.f, 0.f, 0.f, 0.f};
.LBB0_487:
	v_mov_b32_e32 v13, v151
	v_mov_b32_e32 v15, v151
	s_add_u32 s3, s6, 0x100
	v_mov_b32_e32 v34, 0
	v_lshl_add_u64 v[16:17], s[20:21], 0, v[14:15]
	v_lshl_add_u64 v[98:99], s[20:21], 0, v[12:13]
	s_addc_u32 s36, s7, 0
	s_mov_b32 s37, -2
	s_mov_b64 s[6:7], 0
	v_pk_mov_b32 v[2:3], 0, 0
	v_pk_mov_b32 v[4:5], 0, 0
	v_pk_mov_b32 v[6:7], 0, 0
	v_pk_mov_b32 v[8:9], 0, 0
	v_pk_mov_b32 v[18:19], 0, 0
	v_pk_mov_b32 v[20:21], 0, 0
	v_pk_mov_b32 v[22:23], 0, 0
	v_pk_mov_b32 v[24:25], 0, 0
	v_pk_mov_b32 v[26:27], 0, 0
	v_pk_mov_b32 v[28:29], 0, 0
	v_pk_mov_b32 v[30:31], 0, 0
	v_pk_mov_b32 v[32:33], 0, 0
	v_pk_mov_b32 v[34:35], 0, 0
	v_pk_mov_b32 v[36:37], 0, 0
	v_pk_mov_b32 v[38:39], 0, 0
	v_pk_mov_b32 v[40:41], 0, 0
	v_pk_mov_b32 v[42:43], 0, 0
	v_pk_mov_b32 v[44:45], 0, 0
	v_pk_mov_b32 v[46:47], 0, 0
	v_pk_mov_b32 v[48:49], 0, 0
	v_pk_mov_b32 v[50:51], 0, 0
	v_pk_mov_b32 v[52:53], 0, 0
	v_pk_mov_b32 v[54:55], 0, 0
	v_pk_mov_b32 v[56:57], 0, 0
	v_pk_mov_b32 v[58:59], 0, 0
	v_pk_mov_b32 v[60:61], 0, 0
	v_pk_mov_b32 v[62:63], 0, 0
	v_pk_mov_b32 v[64:65], 0, 0
	v_pk_mov_b32 v[66:67], 0, 0
	v_pk_mov_b32 v[68:69], 0, 0
	v_pk_mov_b32 v[70:71], 0, 0
	v_pk_mov_b32 v[72:73], 0, 0
	v_pk_mov_b32 v[74:75], 0, 0
	v_pk_mov_b32 v[76:77], 0, 0
	v_pk_mov_b32 v[78:79], 0, 0
	v_pk_mov_b32 v[80:81], 0, 0
	v_pk_mov_b32 v[82:83], 0, 0
	v_pk_mov_b32 v[84:85], 0, 0
	v_pk_mov_b32 v[86:87], 0, 0
	v_pk_mov_b32 v[88:89], 0, 0
	v_pk_mov_b32 v[90:91], 0, 0
	v_pk_mov_b32 v[92:93], 0, 0
	v_pk_mov_b32 v[94:95], 0, 0
	v_pk_mov_b32 v[96:97], 0, 0
	v_pk_mov_b32 v[102:103], 0, 0
	v_pk_mov_b32 v[104:105], 0, 0
	v_pk_mov_b32 v[110:111], 0, 0
	v_pk_mov_b32 v[112:113], 0, 0
	v_pk_mov_b32 v[114:115], 0, 0
	v_pk_mov_b32 v[116:117], 0, 0
	v_pk_mov_b32 v[118:119], 0, 0
	v_pk_mov_b32 v[120:121], 0, 0
	v_pk_mov_b32 v[122:123], 0, 0
	v_pk_mov_b32 v[124:125], 0, 0
	v_pk_mov_b32 v[126:127], 0, 0
	v_pk_mov_b32 v[128:129], 0, 0
	v_pk_mov_b32 v[130:131], 0, 0
	v_pk_mov_b32 v[132:133], 0, 0
	v_pk_mov_b32 v[134:135], 0, 0
	v_pk_mov_b32 v[136:137], 0, 0
	v_pk_mov_b32 v[138:139], 0, 0
	v_pk_mov_b32 v[140:141], 0, 0
	v_pk_mov_b32 v[142:143], 0, 0
	v_pk_mov_b32 v[144:145], 0, 0

;     ...
; #pragma unroll
;         for (int a = 0; a < 2; ++a)
; #pragma unroll
;             for (int b = 0; b < 2; ++b)
; #pragma unroll
;                 for (int m = 0; m < 4; ++m)
; #pragma unroll
;                     for (int n = 0; n < 2; ++n) acc[a][b][m][n] = (f32x4){0.f, 0.f, 0.f, 0.f};
.LBB0_1489:
	v_lshl_or_b32 v184, s50, 8, v198
	v_mov_b32_e32 v179, v173
	v_mov_b32_e32 v181, v173
	s_add_u32 s92, s66, 0x100
	v_mov_b32_e32 v10, 0
	v_lshl_add_u32 v182, s3, 8, v167
	v_ashrrev_i32_e32 v185, 31, v184
	v_lshl_add_u64 v[186:187], s[22:23], 0, v[180:181]
	v_lshl_add_u64 v[188:189], s[22:23], 0, v[178:179]
	s_addc_u32 s93, s67, 0
	s_mov_b32 s94, -2
	s_mov_b64 s[66:67], 0
	v_pk_mov_b32 v[2:3], 0, 0
	v_pk_mov_b32 v[4:5], 0, 0
	v_pk_mov_b32 v[6:7], 0, 0
	v_pk_mov_b32 v[8:9], 0, 0
	v_pk_mov_b32 v[10:11], 0, 0
	v_pk_mov_b32 v[12:13], 0, 0
	v_pk_mov_b32 v[14:15], 0, 0
	v_pk_mov_b32 v[16:17], 0, 0
	v_pk_mov_b32 v[18:19], 0, 0
	v_pk_mov_b32 v[20:21], 0, 0
	v_pk_mov_b32 v[22:23], 0, 0
	v_pk_mov_b32 v[24:25], 0, 0
	v_pk_mov_b32 v[26:27], 0, 0
	v_pk_mov_b32 v[28:29], 0, 0
	v_pk_mov_b32 v[30:31], 0, 0
	v_pk_mov_b32 v[32:33], 0, 0
	v_pk_mov_b32 v[34:35], 0, 0
	v_pk_mov_b32 v[36:37], 0, 0
	v_pk_mov_b32 v[38:39], 0, 0
	v_pk_mov_b32 v[40:41], 0, 0
	v_pk_mov_b32 v[42:43], 0, 0
	v_pk_mov_b32 v[44:45], 0, 0
	v_pk_mov_b32 v[46:47], 0, 0
	v_pk_mov_b32 v[48:49], 0, 0
	v_pk_mov_b32 v[50:51], 0, 0
	v_pk_mov_b32 v[52:53], 0, 0
	v_pk_mov_b32 v[54:55], 0, 0
	v_pk_mov_b32 v[56:57], 0, 0
	v_pk_mov_b32 v[58:59], 0, 0
	v_pk_mov_b32 v[60:61], 0, 0
	v_pk_mov_b32 v[62:63], 0, 0
	v_pk_mov_b32 v[64:65], 0, 0
	v_pk_mov_b32 v[66:67], 0, 0
	v_pk_mov_b32 v[68:69], 0, 0
	v_pk_mov_b32 v[70:71], 0, 0
	v_pk_mov_b32 v[72:73], 0, 0
	v_pk_mov_b32 v[74:75], 0, 0
	v_pk_mov_b32 v[76:77], 0, 0
	v_pk_mov_b32 v[78:79], 0, 0
	v_pk_mov_b32 v[80:81], 0, 0
	v_pk_mov_b32 v[82:83], 0, 0
	v_pk_mov_b32 v[84:85], 0, 0
	v_pk_mov_b32 v[86:87], 0, 0
	v_pk_mov_b32 v[88:89], 0, 0
	v_pk_mov_b32 v[90:91], 0, 0
	v_pk_mov_b32 v[92:93], 0, 0
	v_pk_mov_b32 v[94:95], 0, 0
	v_pk_mov_b32 v[96:97], 0, 0
	v_pk_mov_b32 v[98:99], 0, 0
	v_pk_mov_b32 v[100:101], 0, 0
	v_pk_mov_b32 v[102:103], 0, 0
	v_pk_mov_b32 v[104:105], 0, 0
	v_pk_mov_b32 v[106:107], 0, 0
	v_pk_mov_b32 v[108:109], 0, 0
	v_pk_mov_b32 v[110:111], 0, 0
	v_pk_mov_b32 v[112:113], 0, 0
	v_pk_mov_b32 v[114:115], 0, 0
	v_pk_mov_b32 v[116:117], 0, 0
	v_pk_mov_b32 v[118:119], 0, 0
	v_pk_mov_b32 v[120:121], 0, 0
	v_pk_mov_b32 v[122:123], 0, 0
	v_pk_mov_b32 v[124:125], 0, 0
	v_pk_mov_b32 v[126:127], 0, 0
	v_pk_mov_b32 v[128:129], 0, 0
	s_branch .LBB0_1491

;     ...
; #pragma unroll
;         for (int a = 0; a < 2; ++a)
; #pragma unroll
;             for (int b = 0; b < 2; ++b)
; #pragma unroll
;                 for (int m = 0; m < 4; ++m)
; #pragma unroll
;                     for (int n = 0; n < 2; ++n) acc[a][b][m][n] = (f32x4){0.f, 0.f, 0.f, 0.f};
.LBB0_1652:
	v_mov_b32_e32 v145, v135
	v_mov_b32_e32 v147, v135
	s_add_u32 s80, s62, 0x100
	v_mov_b32_e32 v22, 0
	v_lshl_add_u64 v[148:149], s[24:25], 0, v[146:147]
	v_lshl_add_u64 v[150:151], s[24:25], 0, v[144:145]
	s_addc_u32 s82, s63, 0
	s_mov_b32 s83, -2
	s_mov_b64 s[62:63], 0
	v_pk_mov_b32 v[2:3], 0, 0
	v_pk_mov_b32 v[4:5], 0, 0
	v_pk_mov_b32 v[6:7], 0, 0
	v_pk_mov_b32 v[8:9], 0, 0
	v_pk_mov_b32 v[10:11], 0, 0
	v_pk_mov_b32 v[12:13], 0, 0
	v_pk_mov_b32 v[14:15], 0, 0
	v_pk_mov_b32 v[16:17], 0, 0
	v_pk_mov_b32 v[18:19], 0, 0
	v_pk_mov_b32 v[20:21], 0, 0
	v_pk_mov_b32 v[22:23], 0, 0
	v_pk_mov_b32 v[24:25], 0, 0
	v_pk_mov_b32 v[26:27], 0, 0
	v_pk_mov_b32 v[28:29], 0, 0
	v_pk_mov_b32 v[30:31], 0, 0
	v_pk_mov_b32 v[32:33], 0, 0
	v_pk_mov_b32 v[34:35], 0, 0
	v_pk_mov_b32 v[36:37], 0, 0
	v_pk_mov_b32 v[38:39], 0, 0
	v_pk_mov_b32 v[40:41], 0, 0
	v_pk_mov_b32 v[42:43], 0, 0
	v_pk_mov_b32 v[44:45], 0, 0
	v_pk_mov_b32 v[46:47], 0, 0
	v_pk_mov_b32 v[48:49], 0, 0
	v_pk_mov_b32 v[50:51], 0, 0
	v_pk_mov_b32 v[52:53], 0, 0
	v_pk_mov_b32 v[54:55], 0, 0
	v_pk_mov_b32 v[56:57], 0, 0
	v_pk_mov_b32 v[58:59], 0, 0
	v_pk_mov_b32 v[60:61], 0, 0
	v_pk_mov_b32 v[62:63], 0, 0
	v_pk_mov_b32 v[64:65], 0, 0
	v_pk_mov_b32 v[66:67], 0, 0
	v_pk_mov_b32 v[68:69], 0, 0
	v_pk_mov_b32 v[70:71], 0, 0
	v_pk_mov_b32 v[72:73], 0, 0
	v_pk_mov_b32 v[74:75], 0, 0
	v_pk_mov_b32 v[76:77], 0, 0
	v_pk_mov_b32 v[78:79], 0, 0
	v_pk_mov_b32 v[80:81], 0, 0
	v_pk_mov_b32 v[82:83], 0, 0
	v_pk_mov_b32 v[84:85], 0, 0
	v_pk_mov_b32 v[86:87], 0, 0
	v_pk_mov_b32 v[88:89], 0, 0
	v_pk_mov_b32 v[90:91], 0, 0
	v_pk_mov_b32 v[92:93], 0, 0
	v_pk_mov_b32 v[94:95], 0, 0
	v_pk_mov_b32 v[96:97], 0, 0
	v_pk_mov_b32 v[98:99], 0, 0
	v_pk_mov_b32 v[100:101], 0, 0
	v_pk_mov_b32 v[102:103], 0, 0
	v_pk_mov_b32 v[104:105], 0, 0
	v_pk_mov_b32 v[106:107], 0, 0
	v_pk_mov_b32 v[108:109], 0, 0
	v_pk_mov_b32 v[110:111], 0, 0
	v_pk_mov_b32 v[112:113], 0, 0
	v_pk_mov_b32 v[114:115], 0, 0
	v_pk_mov_b32 v[116:117], 0, 0
	v_pk_mov_b32 v[118:119], 0, 0
	v_pk_mov_b32 v[120:121], 0, 0
	v_pk_mov_b32 v[122:123], 0, 0
	v_pk_mov_b32 v[124:125], 0, 0
	v_pk_mov_b32 v[126:127], 0, 0
	v_pk_mov_b32 v[128:129], 0, 0

;     ...
;             if constexpr (Sched::GATHER) S.pref(nxt, xgo + ((ui + 1) & 1) * 1024, wid, lane);
;     ...
; #pragma unroll
;         for (int a = 0; a < 2; ++a)
; #pragma unroll
;             for (int b = 0; b < 2; ++b)
; #pragma unroll
;                 for (int m = 0; m < 4; ++m)
; #pragma unroll
;                     for (int n = 0; n < 2; ++n) acc[a][b][m][n] = (f32x4){0.f, 0.f, 0.f, 0.f};
.LBB0_2281:
	s_not_b32 s30, s68
	s_lshl_b32 s30, s30, 10
	s_and_b32 s30, s30, 0x400
	s_add_i32 s30, s30, 0
	s_add_i32 s34, s30, 0x20800
	v_mov_b32_e32 v81, v159
	v_mov_b32_e32 v83, v159
	s_add_u32 s51, s8, 0x100
	v_mov_b32_e32 v30, 0
	v_lshl_add_u64 v[84:85], s[22:23], 0, v[82:83]
	v_lshl_add_u64 v[86:87], s[22:23], 0, v[80:81]
	s_addc_u32 s52, s9, 0
	s_mov_b32 s53, -2
	s_mov_b64 s[30:31], 0
	v_add_u32_e32 v81, s34, v184
	v_add_u32_e32 v83, s34, v185
	v_mov_b32_e32 v189, v79
	v_mov_b32_e32 v191, v78
	v_mov_b32_e32 v190, v80
	v_mov_b32_e32 v192, v82
	v_pk_mov_b32 v[2:3], 0, 0
	v_pk_mov_b32 v[4:5], 0, 0
	v_pk_mov_b32 v[6:7], 0, 0
	v_pk_mov_b32 v[8:9], 0, 0
	v_pk_mov_b32 v[10:11], 0, 0
	v_pk_mov_b32 v[12:13], 0, 0
	v_pk_mov_b32 v[14:15], 0, 0
	v_pk_mov_b32 v[16:17], 0, 0
	v_pk_mov_b32 v[18:19], 0, 0
	v_pk_mov_b32 v[20:21], 0, 0
	v_pk_mov_b32 v[22:23], 0, 0
	v_pk_mov_b32 v[24:25], 0, 0
	v_pk_mov_b32 v[26:27], 0, 0
	v_pk_mov_b32 v[28:29], 0, 0
	v_pk_mov_b32 v[30:31], 0, 0
	v_pk_mov_b32 v[32:33], 0, 0
	v_pk_mov_b32 v[34:35], 0, 0
	v_pk_mov_b32 v[36:37], 0, 0
	v_pk_mov_b32 v[38:39], 0, 0
	v_pk_mov_b32 v[40:41], 0, 0
	v_pk_mov_b32 v[42:43], 0, 0
	v_pk_mov_b32 v[44:45], 0, 0
	v_pk_mov_b32 v[46:47], 0, 0
	v_pk_mov_b32 v[48:49], 0, 0
	v_pk_mov_b32 v[50:51], 0, 0
	v_pk_mov_b32 v[52:53], 0, 0
	v_pk_mov_b32 v[54:55], 0, 0
	v_pk_mov_b32 v[56:57], 0, 0
	v_pk_mov_b32 v[58:59], 0, 0
	v_pk_mov_b32 v[60:61], 0, 0
	v_pk_mov_b32 v[62:63], 0, 0
	v_pk_mov_b32 v[64:65], 0, 0
	v_pk_mov_b32 v[66:67], 0, 0
	v_pk_mov_b32 v[68:69], 0, 0
	v_pk_mov_b32 v[70:71], 0, 0
	v_pk_mov_b32 v[72:73], 0, 0
	v_pk_mov_b32 v[74:75], 0, 0
	v_pk_mov_b32 v[76:77], 0, 0
	v_pk_mov_b32 v[90:91], 0, 0
	v_pk_mov_b32 v[92:93], 0, 0
	v_pk_mov_b32 v[94:95], 0, 0
	v_pk_mov_b32 v[96:97], 0, 0
	v_pk_mov_b32 v[110:111], 0, 0
	v_pk_mov_b32 v[112:113], 0, 0
	v_pk_mov_b32 v[114:115], 0, 0
	v_pk_mov_b32 v[116:117], 0, 0
	v_pk_mov_b32 v[118:119], 0, 0
	v_pk_mov_b32 v[120:121], 0, 0
	v_pk_mov_b32 v[122:123], 0, 0
	v_pk_mov_b32 v[124:125], 0, 0
	v_pk_mov_b32 v[126:127], 0, 0
	v_pk_mov_b32 v[128:129], 0, 0
	v_pk_mov_b32 v[130:131], 0, 0
	v_pk_mov_b32 v[132:133], 0, 0
	v_pk_mov_b32 v[134:135], 0, 0
	v_pk_mov_b32 v[136:137], 0, 0
	v_pk_mov_b32 v[138:139], 0, 0
	v_pk_mov_b32 v[140:141], 0, 0
	v_pk_mov_b32 v[142:143], 0, 0
	v_pk_mov_b32 v[144:145], 0, 0
	v_pk_mov_b32 v[146:147], 0, 0
	v_pk_mov_b32 v[148:149], 0, 0
	v_pk_mov_b32 v[150:151], 0, 0
	v_pk_mov_b32 v[152:153], 0, 0
	s_branch .LBB0_2283

;     ...
; #pragma unroll
;         for (int a = 0; a < 2; ++a)
; #pragma unroll
;             for (int b = 0; b < 2; ++b)
; #pragma unroll
;                 for (int m = 0; m < 4; ++m)
; #pragma unroll
;                     for (int n = 0; n < 2; ++n) acc[a][b][m][n] = (f32x4){0.f, 0.f, 0.f, 0.f};
.LBB0_2450:
	v_mov_b32_e32 v119, v157
	v_mov_b32_e32 v125, v157
	s_add_u32 s50, s38, 0x100
	v_mov_b32_e32 v24, 0
	v_lshl_add_u64 v[126:127], s[30:31], 0, v[124:125]
	v_lshl_add_u64 v[136:137], s[30:31], 0, v[118:119]
	s_addc_u32 s51, s39, 0
	s_mov_b32 s52, -2
	s_mov_b64 s[38:39], 0
	v_pk_mov_b32 v[0:1], 0, 0
	v_pk_mov_b32 v[2:3], 0, 0
	v_pk_mov_b32 v[4:5], 0, 0
	v_pk_mov_b32 v[6:7], 0, 0
	v_pk_mov_b32 v[8:9], 0, 0
	v_pk_mov_b32 v[10:11], 0, 0
	v_pk_mov_b32 v[12:13], 0, 0
	v_pk_mov_b32 v[14:15], 0, 0
	v_pk_mov_b32 v[16:17], 0, 0
	v_pk_mov_b32 v[18:19], 0, 0
	v_pk_mov_b32 v[20:21], 0, 0
	v_pk_mov_b32 v[22:23], 0, 0
	v_pk_mov_b32 v[24:25], 0, 0
	v_pk_mov_b32 v[26:27], 0, 0
	v_pk_mov_b32 v[28:29], 0, 0
	v_pk_mov_b32 v[30:31], 0, 0
	v_pk_mov_b32 v[32:33], 0, 0
	v_pk_mov_b32 v[34:35], 0, 0
	v_pk_mov_b32 v[36:37], 0, 0
	v_pk_mov_b32 v[38:39], 0, 0
	v_pk_mov_b32 v[40:41], 0, 0
	v_pk_mov_b32 v[42:43], 0, 0
	v_pk_mov_b32 v[44:45], 0, 0
	v_pk_mov_b32 v[46:47], 0, 0
	v_pk_mov_b32 v[48:49], 0, 0
	v_pk_mov_b32 v[50:51], 0, 0
	v_pk_mov_b32 v[52:53], 0, 0
	v_pk_mov_b32 v[54:55], 0, 0
	v_pk_mov_b32 v[56:57], 0, 0
	v_pk_mov_b32 v[58:59], 0, 0
	v_pk_mov_b32 v[60:61], 0, 0
	v_pk_mov_b32 v[62:63], 0, 0
	v_pk_mov_b32 v[64:65], 0, 0
	v_pk_mov_b32 v[66:67], 0, 0
	v_pk_mov_b32 v[68:69], 0, 0
	v_pk_mov_b32 v[70:71], 0, 0
	v_pk_mov_b32 v[72:73], 0, 0
	v_pk_mov_b32 v[74:75], 0, 0
	v_pk_mov_b32 v[76:77], 0, 0
	v_pk_mov_b32 v[78:79], 0, 0
	v_pk_mov_b32 v[80:81], 0, 0
	v_pk_mov_b32 v[82:83], 0, 0
	v_pk_mov_b32 v[84:85], 0, 0
	v_pk_mov_b32 v[86:87], 0, 0
	v_pk_mov_b32 v[88:89], 0, 0
	v_pk_mov_b32 v[90:91], 0, 0
	v_pk_mov_b32 v[92:93], 0, 0
	v_pk_mov_b32 v[94:95], 0, 0
	v_pk_mov_b32 v[96:97], 0, 0
	v_pk_mov_b32 v[98:99], 0, 0
	v_pk_mov_b32 v[100:101], 0, 0
	v_pk_mov_b32 v[102:103], 0, 0
	v_pk_mov_b32 v[104:105], 0, 0
	v_pk_mov_b32 v[106:107], 0, 0
	v_pk_mov_b32 v[108:109], 0, 0
	v_pk_mov_b32 v[110:111], 0, 0
	v_pk_mov_b32 v[112:113], 0, 0
	v_pk_mov_b32 v[114:115], 0, 0
	v_pk_mov_b32 v[120:121], 0, 0
	v_pk_mov_b32 v[122:123], 0, 0
	v_pk_mov_b32 v[128:129], 0, 0
	v_pk_mov_b32 v[130:131], 0, 0
	v_pk_mov_b32 v[132:133], 0, 0
	v_pk_mov_b32 v[134:135], 0, 0
